# attention QK^T ds_read software-pipelined 8 deep in compressed/selected/window branches; dropped compiler vmcnt(0) in compressed tile loop
# speedup vs baseline: 1.0106x; 1.0106x over previous
; #define LAS __attribute__((address_space(3)))
; __device__ __forceinline__ void at_qkt(f32x16& p0, f32x16& p1, const LAS unsigned char* Kt, int l32, int hi, const bf16x8 (&qr)[8], const f32x16& cinit) {
;     const LAS unsigned char* kb[4];
; #pragma unroll
;     for (int dd = 0; dd < 4; ++dd) kb[dd] = Kt + KSWZ(l32, (dd * 16 + hi * 8) * 2);
; #pragma unroll
;     for (int d0 = 0; d0 < 8; ++d0) { const LAS unsigned char* a = kb[d0 & 3] + (d0 >> 2) * 128;
;         const bf16x8 b0 = *(const LAS bf16x8*)a, b1 = *(const LAS bf16x8*)(a + 32 * 256);
;         if (d0 == 0) { p0 = __builtin_amdgcn_mfma_f32_32x32x16_bf16(b0, qr[0], cinit, 0, 0, 0); p1 = __builtin_amdgcn_mfma_f32_32x32x16_bf16(b1, qr[0], cinit, 0, 0, 0); }
;         else { p0 = __builtin_amdgcn_mfma_f32_32x32x16_bf16(b0, qr[d0], p0, 0, 0, 0); p1 = __builtin_amdgcn_mfma_f32_32x32x16_bf16(b1, qr[d0], p1, 0, 0, 0); } }
; }
; template <int MODE>
; __device__ __forceinline__ void at_mask(f32x16& p0, f32x16& p1, int kb, int hi, int tq, int lim, bool rowsel) {
;     const float NEG = -__builtin_inff();
; #pragma unroll
;     for (int r = 0; r < 16; ++r) { const int k0 = kb + (r & 3) + 8 * (r >> 2) + 4 * hi, k1 = k0 + 32;
;         bool v0, v1;
;         if (MODE == 0) { v0 = k0 <= lim; v1 = k1 <= lim; }
;         else if (MODE == 1) { v0 = rowsel && k0 <= tq; v1 = rowsel && k1 <= tq; }
;         else { v0 = (unsigned)(tq - k0) < (unsigned)WIN; v1 = (unsigned)(tq - k1) < (unsigned)WIN; }
;         if (!v0) p0[r] = NEG; if (!v1) p1[r] = NEG; }
; }
.LBB0_802:
	v_add_u32_e32 v2, s30, v128
	v_add_u32_e32 v164, v2, v129
	v_add_u32_e32 v165, v2, v180
	v_add_u32_e32 v166, v2, v181
	v_add_u32_e32 v2, v2, v182
	ds_read_b128 v[170:173], v164
	ds_read_b128 v[202:205], v164 offset:8192
	ds_read_b128 v[206:209], v165
	ds_read_b128 v[210:213], v165 offset:8192
	ds_read_b128 v[232:235], v166
	ds_read_b128 v[236:239], v166 offset:8192
	ds_read_b128 v[240:243], v2
	ds_read_b128 v[244:247], v2 offset:8192
	s_cmp_le_i32 s20, s18
	s_waitcnt lgkmcnt(7)
	v_mfma_f32_32x32x16_bf16 v[100:115], v[170:173], v[130:133], v[68:83]
	ds_read_b128 v[170:173], v164 offset:128
	s_waitcnt lgkmcnt(7)
	v_mfma_f32_32x32x16_bf16 v[84:99], v[202:205], v[130:133], v[68:83]
	ds_read_b128 v[202:205], v164 offset:8320
	s_waitcnt lgkmcnt(7)
	v_mfma_f32_32x32x16_bf16 v[100:115], v[206:209], v[134:137], v[100:115]
	ds_read_b128 v[206:209], v165 offset:128
	s_waitcnt lgkmcnt(7)
	v_mfma_f32_32x32x16_bf16 v[84:99], v[210:213], v[134:137], v[84:99]
	ds_read_b128 v[210:213], v165 offset:8320
	s_waitcnt lgkmcnt(7)
	v_mfma_f32_32x32x16_bf16 v[100:115], v[232:235], v[138:141], v[100:115]
	ds_read_b128 v[232:235], v166 offset:128
	s_waitcnt lgkmcnt(7)
	v_mfma_f32_32x32x16_bf16 v[84:99], v[236:239], v[138:141], v[84:99]
	ds_read_b128 v[236:239], v166 offset:8320
	s_waitcnt lgkmcnt(7)
	v_mfma_f32_32x32x16_bf16 v[100:115], v[240:243], v[142:145], v[100:115]
	ds_read_b128 v[240:243], v2 offset:128
	s_waitcnt lgkmcnt(7)
	v_mfma_f32_32x32x16_bf16 v[84:99], v[244:247], v[142:145], v[84:99]
	ds_read_b128 v[244:247], v2 offset:8320
	s_waitcnt lgkmcnt(7)
	v_mfma_f32_32x32x16_bf16 v[100:115], v[170:173], v[146:149], v[100:115]
	s_waitcnt lgkmcnt(6)
	v_mfma_f32_32x32x16_bf16 v[84:99], v[202:205], v[146:149], v[84:99]
	s_waitcnt lgkmcnt(5)
	v_mfma_f32_32x32x16_bf16 v[100:115], v[206:209], v[150:153], v[100:115]
	s_waitcnt lgkmcnt(4)
	v_mfma_f32_32x32x16_bf16 v[84:99], v[210:213], v[150:153], v[84:99]
	s_waitcnt lgkmcnt(3)
	v_mfma_f32_32x32x16_bf16 v[100:115], v[232:235], v[154:157], v[100:115]
	s_waitcnt lgkmcnt(2)
	v_mfma_f32_32x32x16_bf16 v[84:99], v[236:239], v[154:157], v[84:99]
	s_waitcnt lgkmcnt(1)
	v_mfma_f32_32x32x16_bf16 v[100:115], v[240:243], v[158:161], v[100:115]
	s_waitcnt lgkmcnt(0)
	v_mfma_f32_32x32x16_bf16 v[84:99], v[244:247], v[158:161], v[84:99]
	s_cbranch_scc1 .LBB0_804
	v_add_u32_e32 v2, s20, v183
	v_subrev_u32_e32 v164, 63, v2
	v_cmp_lt_i32_e32 vcc, v164, v1
	s_nop 4
	v_cndmask_b32_e32 v101, v226, v101, vcc
	v_cmp_le_i32_e32 vcc, v164, v1
	s_nop 1
	v_cndmask_b32_e32 v100, v226, v100, vcc
	v_cmp_lt_i32_e32 vcc, v164, v121
	s_nop 1
	v_cndmask_b32_e32 v85, v226, v85, vcc
	v_cmp_le_i32_e32 vcc, v164, v121
	v_subrev_u32_e32 v164, 61, v2
	s_nop 0
	v_cndmask_b32_e32 v84, v226, v84, vcc
	v_cmp_le_i32_e32 vcc, v164, v1
	s_nop 1
	v_cndmask_b32_e32 v102, v226, v102, vcc
	v_cmp_le_i32_e32 vcc, v164, v121
	v_subrev_u32_e32 v164, 60, v2
	s_nop 0
	v_cndmask_b32_e32 v86, v226, v86, vcc
	v_cmp_le_i32_e32 vcc, v164, v1
	s_nop 1
	v_cndmask_b32_e32 v103, v226, v103, vcc
	v_cmp_le_i32_e32 vcc, v164, v121
	v_subrev_u32_e32 v164, 55, v2
	s_nop 0
	v_cndmask_b32_e32 v87, v226, v87, vcc
	v_cmp_le_i32_e32 vcc, v164, v1
	s_nop 1
	v_cndmask_b32_e32 v104, v226, v104, vcc
	v_cmp_le_i32_e32 vcc, v164, v121
	v_subrev_u32_e32 v164, 54, v2
	s_nop 0
	v_cndmask_b32_e32 v88, v226, v88, vcc
	v_cmp_le_i32_e32 vcc, v164, v1
	s_nop 1
	v_cndmask_b32_e32 v105, v226, v105, vcc
	v_cmp_le_i32_e32 vcc, v164, v121
	v_subrev_u32_e32 v164, 53, v2
	s_nop 0
	v_cndmask_b32_e32 v89, v226, v89, vcc
	v_cmp_le_i32_e32 vcc, v164, v1
	s_nop 1
	v_cndmask_b32_e32 v106, v226, v106, vcc
	v_cmp_le_i32_e32 vcc, v164, v121
	v_subrev_u32_e32 v164, 52, v2
	s_nop 0
	v_cndmask_b32_e32 v90, v226, v90, vcc
	v_cmp_le_i32_e32 vcc, v164, v1
	s_nop 1
	v_cndmask_b32_e32 v107, v226, v107, vcc
	v_cmp_le_i32_e32 vcc, v164, v121
	v_subrev_u32_e32 v164, 47, v2
	s_nop 0
	v_cndmask_b32_e32 v91, v226, v91, vcc
	v_cmp_le_i32_e32 vcc, v164, v1
	s_nop 1
	v_cndmask_b32_e32 v108, v226, v108, vcc
	v_cmp_le_i32_e32 vcc, v164, v121
	v_subrev_u32_e32 v164, 46, v2
	s_nop 0
	v_cndmask_b32_e32 v92, v226, v92, vcc
	v_cmp_le_i32_e32 vcc, v164, v1
	s_nop 1
	v_cndmask_b32_e32 v109, v226, v109, vcc
	v_cmp_le_i32_e32 vcc, v164, v121
	v_subrev_u32_e32 v164, 45, v2
	s_nop 0
	v_cndmask_b32_e32 v93, v226, v93, vcc
	v_cmp_le_i32_e32 vcc, v164, v1
	s_nop 1
	v_cndmask_b32_e32 v110, v226, v110, vcc
	v_cmp_le_i32_e32 vcc, v164, v121
	v_subrev_u32_e32 v164, 44, v2
	s_nop 0
	v_cndmask_b32_e32 v94, v226, v94, vcc
	v_cmp_le_i32_e32 vcc, v164, v1
	s_nop 1
	v_cndmask_b32_e32 v111, v226, v111, vcc
	v_cmp_le_i32_e32 vcc, v164, v121
	v_subrev_u32_e32 v164, 39, v2
	s_nop 0
	v_cndmask_b32_e32 v95, v226, v95, vcc
	v_cmp_le_i32_e32 vcc, v164, v1
	s_nop 1
	v_cndmask_b32_e32 v112, v226, v112, vcc
	v_cmp_le_i32_e32 vcc, v164, v121
	v_subrev_u32_e32 v164, 38, v2
	s_nop 0
	v_cndmask_b32_e32 v96, v226, v96, vcc
	v_cmp_le_i32_e32 vcc, v164, v1
	s_nop 1
	v_cndmask_b32_e32 v113, v226, v113, vcc
	v_cmp_le_i32_e32 vcc, v164, v121
	v_subrev_u32_e32 v164, 37, v2
	v_subrev_u32_e32 v2, 36, v2
	v_cndmask_b32_e32 v97, v226, v97, vcc
	v_cmp_le_i32_e32 vcc, v164, v1
	s_nop 1
	v_cndmask_b32_e32 v114, v226, v114, vcc
	v_cmp_le_i32_e32 vcc, v164, v121
	s_nop 1
	v_cndmask_b32_e32 v98, v226, v98, vcc
	v_cmp_le_i32_e32 vcc, v2, v1
	s_nop 1
	v_cndmask_b32_e32 v115, v226, v115, vcc
	v_cmp_le_i32_e32 vcc, v2, v121
	s_nop 1
	v_cndmask_b32_e32 v99, v226, v99, vcc

; #define LAS __attribute__((address_space(3)))
; __device__ __forceinline__ void at_qkt(f32x16& p0, f32x16& p1, const LAS unsigned char* Kt, int l32, int hi, const bf16x8 (&qr)[8], const f32x16& cinit) {
;     const LAS unsigned char* kb[4];
; #pragma unroll
;     for (int dd = 0; dd < 4; ++dd) kb[dd] = Kt + KSWZ(l32, (dd * 16 + hi * 8) * 2);
; #pragma unroll
;     for (int d0 = 0; d0 < 8; ++d0) { const LAS unsigned char* a = kb[d0 & 3] + (d0 >> 2) * 128;
;         const bf16x8 b0 = *(const LAS bf16x8*)a, b1 = *(const LAS bf16x8*)(a + 32 * 256);
;         if (d0 == 0) { p0 = __builtin_amdgcn_mfma_f32_32x32x16_bf16(b0, qr[0], cinit, 0, 0, 0); p1 = __builtin_amdgcn_mfma_f32_32x32x16_bf16(b1, qr[0], cinit, 0, 0, 0); }
;         else { p0 = __builtin_amdgcn_mfma_f32_32x32x16_bf16(b0, qr[d0], p0, 0, 0, 0); p1 = __builtin_amdgcn_mfma_f32_32x32x16_bf16(b1, qr[d0], p1, 0, 0, 0); } }
; }
; template <int MODE>
; __device__ __forceinline__ void at_mask(f32x16& p0, f32x16& p1, int kb, int hi, int tq, int lim, bool rowsel) {
;     const float NEG = -__builtin_inff();
; #pragma unroll
;     for (int r = 0; r < 16; ++r) { const int k0 = kb + (r & 3) + 8 * (r >> 2) + 4 * hi, k1 = k0 + 32;
;         bool v0, v1;
;         if (MODE == 0) { v0 = k0 <= lim; v1 = k1 <= lim; }
;         else if (MODE == 1) { v0 = rowsel && k0 <= tq; v1 = rowsel && k1 <= tq; }
;         else { v0 = (unsigned)(tq - k0) < (unsigned)WIN; v1 = (unsigned)(tq - k1) < (unsigned)WIN; }
;         if (!v0) p0[r] = NEG; if (!v1) p1[r] = NEG; }
; }
.LBB0_848:
	s_lshr_b32 s0, s16, 3
	s_and_b32 s0, s0, 0x1ffffffc
	v_add_u32_e32 v2, s0, v191
	ds_read_b32 v2, v2
	s_and_b32 s0, s16, 31
	s_waitcnt lgkmcnt(0)
	v_lshrrev_b32_e32 v4, s16, v2
	v_bfe_u32 v2, v2, s0, 1
	v_and_b32_e32 v4, 1, v4
	v_cmp_ne_u32_e32 vcc, 0, v2
	v_cmp_eq_u32_e64 s[6:7], 1, v4
	s_cbranch_vccz .LBB0_859
	s_lshl_b32 s17, s14, 14
	v_add_u32_e32 v2, s17, v193
	v_add_u32_e32 v8, v2, v194
	v_add_u32_e32 v9, v2, v195
	v_add_u32_e32 v10, v2, v196
	v_add_u32_e32 v2, v2, v197
	ds_read_b128 v[4:7], v8
	ds_read_b128 v[202:205], v8 offset:8192
	ds_read_b128 v[206:209], v9
	ds_read_b128 v[210:213], v9 offset:8192
	ds_read_b128 v[232:235], v10
	ds_read_b128 v[236:239], v10 offset:8192
	ds_read_b128 v[240:243], v2
	ds_read_b128 v[244:247], v2 offset:8192
	s_cmp_le_i32 s15, s11
	s_waitcnt lgkmcnt(7)
	v_mfma_f32_32x32x16_bf16 v[114:129], v[4:7], v[130:133], v[82:97]
	ds_read_b128 v[4:7], v8 offset:128
	s_waitcnt lgkmcnt(7)
	v_mfma_f32_32x32x16_bf16 v[98:113], v[202:205], v[130:133], v[82:97]
	ds_read_b128 v[202:205], v8 offset:8320
	s_waitcnt lgkmcnt(7)
	v_mfma_f32_32x32x16_bf16 v[114:129], v[206:209], v[134:137], v[114:129]
	ds_read_b128 v[206:209], v9 offset:128
	s_waitcnt lgkmcnt(7)
	v_mfma_f32_32x32x16_bf16 v[98:113], v[210:213], v[134:137], v[98:113]
	ds_read_b128 v[210:213], v9 offset:8320
	s_waitcnt lgkmcnt(7)
	v_mfma_f32_32x32x16_bf16 v[114:129], v[232:235], v[138:141], v[114:129]
	ds_read_b128 v[232:235], v10 offset:128
	s_waitcnt lgkmcnt(7)
	v_mfma_f32_32x32x16_bf16 v[98:113], v[236:239], v[138:141], v[98:113]
	ds_read_b128 v[236:239], v10 offset:8320
	s_waitcnt lgkmcnt(7)
	v_mfma_f32_32x32x16_bf16 v[114:129], v[240:243], v[142:145], v[114:129]
	ds_read_b128 v[240:243], v2 offset:128
	s_waitcnt lgkmcnt(7)
	v_mfma_f32_32x32x16_bf16 v[98:113], v[244:247], v[142:145], v[98:113]
	ds_read_b128 v[244:247], v2 offset:8320
	s_waitcnt lgkmcnt(7)
	v_mfma_f32_32x32x16_bf16 v[114:129], v[4:7], v[146:149], v[114:129]
	s_waitcnt lgkmcnt(6)
	v_mfma_f32_32x32x16_bf16 v[98:113], v[202:205], v[146:149], v[98:113]
	s_waitcnt lgkmcnt(5)
	v_mfma_f32_32x32x16_bf16 v[114:129], v[206:209], v[150:153], v[114:129]
	s_waitcnt lgkmcnt(4)
	v_mfma_f32_32x32x16_bf16 v[98:113], v[210:213], v[150:153], v[98:113]
	s_waitcnt lgkmcnt(3)
	v_mfma_f32_32x32x16_bf16 v[114:129], v[232:235], v[154:157], v[114:129]
	s_waitcnt lgkmcnt(2)
	v_mfma_f32_32x32x16_bf16 v[98:113], v[236:239], v[154:157], v[98:113]
	s_waitcnt lgkmcnt(1)
	v_mfma_f32_32x32x16_bf16 v[114:129], v[240:243], v[158:161], v[114:129]
	s_waitcnt lgkmcnt(0)
	v_mfma_f32_32x32x16_bf16 v[98:113], v[244:247], v[158:161], v[98:113]
	s_cbranch_scc1 .LBB0_851
	v_add_u32_e32 v2, s15, v198
	v_subrev_u32_e32 v5, 31, v2
	v_subrev_u32_e32 v4, 63, v2
	v_cmp_le_i32_e32 vcc, v5, v187
	v_subrev_u32_e32 v5, 30, v2
	s_nop 5
	v_cndmask_b32_e32 v98, v226, v98, vcc
	v_cmp_lt_i32_e32 vcc, v4, v187
	s_nop 1
	v_cndmask_b32_e32 v115, v226, v115, vcc
	v_cmp_le_i32_e32 vcc, v4, v187
	v_subrev_u32_e32 v4, 61, v2
	s_nop 0
	v_cndmask_b32_e32 v114, v226, v114, vcc
	v_cmp_le_i32_e32 vcc, v5, v187
	v_subrev_u32_e32 v5, 29, v2
	s_nop 0
	v_cndmask_b32_e32 v99, v226, v99, vcc
	v_cmp_le_i32_e32 vcc, v4, v187
	v_subrev_u32_e32 v4, 60, v2
	s_nop 0
	v_cndmask_b32_e32 v116, v226, v116, vcc
	v_cmp_le_i32_e32 vcc, v5, v187
	v_subrev_u32_e32 v5, 28, v2
	s_nop 0
	v_cndmask_b32_e32 v100, v226, v100, vcc
	v_cmp_le_i32_e32 vcc, v4, v187
	v_subrev_u32_e32 v4, 55, v2
	s_nop 0
	v_cndmask_b32_e32 v117, v226, v117, vcc
	v_cmp_le_i32_e32 vcc, v5, v187
	v_subrev_u32_e32 v5, 23, v2
	s_nop 0
	v_cndmask_b32_e32 v101, v226, v101, vcc
	v_cmp_le_i32_e32 vcc, v4, v187
	v_subrev_u32_e32 v4, 54, v2
	s_nop 0
	v_cndmask_b32_e32 v118, v226, v118, vcc
	v_cmp_le_i32_e32 vcc, v5, v187
	v_subrev_u32_e32 v5, 22, v2
	s_nop 0
	v_cndmask_b32_e32 v102, v226, v102, vcc
	v_cmp_le_i32_e32 vcc, v4, v187
	v_subrev_u32_e32 v4, 53, v2
	s_nop 0
	v_cndmask_b32_e32 v119, v226, v119, vcc
	v_cmp_le_i32_e32 vcc, v5, v187
	v_subrev_u32_e32 v5, 21, v2
	s_nop 0
	v_cndmask_b32_e32 v103, v226, v103, vcc
	v_cmp_le_i32_e32 vcc, v4, v187
	v_subrev_u32_e32 v4, 52, v2
	s_nop 0
	v_cndmask_b32_e32 v120, v226, v120, vcc
	v_cmp_le_i32_e32 vcc, v5, v187
	v_subrev_u32_e32 v5, 20, v2
	s_nop 0
	v_cndmask_b32_e32 v104, v226, v104, vcc
	v_cmp_le_i32_e32 vcc, v4, v187
	v_subrev_u32_e32 v4, 47, v2
	s_nop 0
	v_cndmask_b32_e32 v121, v226, v121, vcc
	v_cmp_le_i32_e32 vcc, v5, v187
	v_add_u32_e32 v5, -15, v2
	s_nop 0
	v_cndmask_b32_e32 v105, v226, v105, vcc
	v_cmp_le_i32_e32 vcc, v4, v187
	v_subrev_u32_e32 v4, 46, v2
	s_nop 0
	v_cndmask_b32_e32 v122, v226, v122, vcc
	v_cmp_le_i32_e32 vcc, v5, v187
	v_add_u32_e32 v5, -14, v2
	s_nop 0
	v_cndmask_b32_e32 v106, v226, v106, vcc
	v_cmp_le_i32_e32 vcc, v4, v187
	v_subrev_u32_e32 v4, 45, v2
	s_nop 0
	v_cndmask_b32_e32 v123, v226, v123, vcc
	v_cmp_le_i32_e32 vcc, v5, v187
	v_add_u32_e32 v5, -13, v2
	s_nop 0
	v_cndmask_b32_e32 v107, v226, v107, vcc
	v_cmp_le_i32_e32 vcc, v4, v187
	v_subrev_u32_e32 v4, 44, v2
	s_nop 0
	v_cndmask_b32_e32 v124, v226, v124, vcc
	v_cmp_le_i32_e32 vcc, v5, v187
	v_add_u32_e32 v5, -12, v2
	s_nop 0
	v_cndmask_b32_e32 v108, v226, v108, vcc
	v_cmp_le_i32_e32 vcc, v4, v187
	v_subrev_u32_e32 v4, 39, v2
	s_nop 0
	v_cndmask_b32_e32 v125, v226, v125, vcc
	v_cmp_le_i32_e32 vcc, v5, v187
	v_add_u32_e32 v5, -7, v2
	s_nop 0
	v_cndmask_b32_e32 v109, v226, v109, vcc
	v_cmp_le_i32_e32 vcc, v4, v187
	v_subrev_u32_e32 v4, 38, v2
	s_nop 0
	v_cndmask_b32_e32 v126, v226, v126, vcc
	v_cmp_le_i32_e32 vcc, v5, v187
	v_add_u32_e32 v5, -6, v2
	s_nop 0
	v_cndmask_b32_e32 v110, v226, v110, vcc
	v_cmp_le_i32_e32 vcc, v4, v187
	v_subrev_u32_e32 v4, 37, v2
	s_nop 0
	v_cndmask_b32_e32 v127, v226, v127, vcc
	v_cmp_le_i32_e32 vcc, v5, v187
	v_add_u32_e32 v5, -5, v2
	s_nop 0
	v_cndmask_b32_e32 v111, v226, v111, vcc
	v_cmp_le_i32_e32 vcc, v4, v187
	v_subrev_u32_e32 v4, 36, v2
	v_add_u32_e32 v2, -4, v2
	v_cndmask_b32_e32 v128, v226, v128, vcc
	v_cmp_le_i32_e32 vcc, v5, v187
	s_nop 1
	v_cndmask_b32_e32 v112, v226, v112, vcc
	v_cmp_le_i32_e32 vcc, v4, v187
	s_nop 1
	v_cndmask_b32_e32 v129, v226, v129, vcc
	v_cmp_le_i32_e32 vcc, v2, v187
	s_nop 1
	v_cndmask_b32_e32 v113, v226, v113, vcc

; #define LAS __attribute__((address_space(3)))
; __device__ __forceinline__ void at_qkt(f32x16& p0, f32x16& p1, const LAS unsigned char* Kt, int l32, int hi, const bf16x8 (&qr)[8], const f32x16& cinit) {
;     const LAS unsigned char* kb[4];
; #pragma unroll
;     for (int dd = 0; dd < 4; ++dd) kb[dd] = Kt + KSWZ(l32, (dd * 16 + hi * 8) * 2);
; #pragma unroll
;     for (int d0 = 0; d0 < 8; ++d0) { const LAS unsigned char* a = kb[d0 & 3] + (d0 >> 2) * 128;
;         const bf16x8 b0 = *(const LAS bf16x8*)a, b1 = *(const LAS bf16x8*)(a + 32 * 256);
;         if (d0 == 0) { p0 = __builtin_amdgcn_mfma_f32_32x32x16_bf16(b0, qr[0], cinit, 0, 0, 0); p1 = __builtin_amdgcn_mfma_f32_32x32x16_bf16(b1, qr[0], cinit, 0, 0, 0); }
;         else { p0 = __builtin_amdgcn_mfma_f32_32x32x16_bf16(b0, qr[d0], p0, 0, 0, 0); p1 = __builtin_amdgcn_mfma_f32_32x32x16_bf16(b1, qr[d0], p1, 0, 0, 0); } }
; }
; template <int MODE>
; __device__ __forceinline__ void at_mask(f32x16& p0, f32x16& p1, int kb, int hi, int tq, int lim, bool rowsel) {
;     const float NEG = -__builtin_inff();
; #pragma unroll
;     for (int r = 0; r < 16; ++r) { const int k0 = kb + (r & 3) + 8 * (r >> 2) + 4 * hi, k1 = k0 + 32;
;         bool v0, v1;
;         if (MODE == 0) { v0 = k0 <= lim; v1 = k1 <= lim; }
;         else if (MODE == 1) { v0 = rowsel && k0 <= tq; v1 = rowsel && k1 <= tq; }
;         else { v0 = (unsigned)(tq - k0) < (unsigned)WIN; v1 = (unsigned)(tq - k1) < (unsigned)WIN; }
;         if (!v0) p0[r] = NEG; if (!v1) p1[r] = NEG; }
; }
.LBB0_875:
	v_add_u32_e32 v2, s20, v124
	v_add_u32_e32 v164, v2, v125
	v_add_u32_e32 v165, v2, v126
	v_add_u32_e32 v166, v2, v127
	v_add_u32_e32 v2, v2, v128
	ds_read_b128 v[170:173], v164
	ds_read_b128 v[202:205], v164 offset:8192
	ds_read_b128 v[206:209], v165
	ds_read_b128 v[210:213], v165 offset:8192
	ds_read_b128 v[232:235], v166
	ds_read_b128 v[236:239], v166 offset:8192
	ds_read_b128 v[240:243], v2
	ds_read_b128 v[244:247], v2 offset:8192
	s_add_i32 s0, s17, 63
	s_cmp_gt_i32 s0, s11
	s_cselect_b64 s[0:1], -1, 0
	s_cmp_le_i32 s17, s15
	s_cselect_b64 s[30:31], -1, 0
	s_or_b64 s[0:1], s[0:1], s[30:31]
	s_andn2_b64 vcc, exec, s[0:1]
	s_waitcnt lgkmcnt(7)
	v_mfma_f32_32x32x16_bf16 v[100:115], v[170:173], v[130:133], v[68:83]
	ds_read_b128 v[170:173], v164 offset:128
	s_waitcnt lgkmcnt(7)
	v_mfma_f32_32x32x16_bf16 v[84:99], v[202:205], v[130:133], v[68:83]
	ds_read_b128 v[202:205], v164 offset:8320
	s_waitcnt lgkmcnt(7)
	v_mfma_f32_32x32x16_bf16 v[100:115], v[206:209], v[134:137], v[100:115]
	ds_read_b128 v[206:209], v165 offset:128
	s_waitcnt lgkmcnt(7)
	v_mfma_f32_32x32x16_bf16 v[84:99], v[210:213], v[134:137], v[84:99]
	ds_read_b128 v[210:213], v165 offset:8320
	s_waitcnt lgkmcnt(7)
	v_mfma_f32_32x32x16_bf16 v[100:115], v[232:235], v[138:141], v[100:115]
	ds_read_b128 v[232:235], v166 offset:128
	s_waitcnt lgkmcnt(7)
	v_mfma_f32_32x32x16_bf16 v[84:99], v[236:239], v[138:141], v[84:99]
	ds_read_b128 v[236:239], v166 offset:8320
	s_waitcnt lgkmcnt(7)
	v_mfma_f32_32x32x16_bf16 v[100:115], v[240:243], v[142:145], v[100:115]
	ds_read_b128 v[240:243], v2 offset:128
	s_waitcnt lgkmcnt(7)
	v_mfma_f32_32x32x16_bf16 v[84:99], v[244:247], v[142:145], v[84:99]
	ds_read_b128 v[244:247], v2 offset:8320
	s_waitcnt lgkmcnt(7)
	v_mfma_f32_32x32x16_bf16 v[100:115], v[170:173], v[146:149], v[100:115]
	s_waitcnt lgkmcnt(6)
	v_mfma_f32_32x32x16_bf16 v[84:99], v[202:205], v[146:149], v[84:99]
	s_waitcnt lgkmcnt(5)
	v_mfma_f32_32x32x16_bf16 v[100:115], v[206:209], v[150:153], v[100:115]
	s_waitcnt lgkmcnt(4)
	v_mfma_f32_32x32x16_bf16 v[84:99], v[210:213], v[150:153], v[84:99]
	s_waitcnt lgkmcnt(3)
	v_mfma_f32_32x32x16_bf16 v[100:115], v[232:235], v[154:157], v[100:115]
	s_waitcnt lgkmcnt(2)
	v_mfma_f32_32x32x16_bf16 v[84:99], v[236:239], v[154:157], v[84:99]
	s_waitcnt lgkmcnt(1)
	v_mfma_f32_32x32x16_bf16 v[100:115], v[240:243], v[158:161], v[100:115]
	s_waitcnt lgkmcnt(0)
	v_mfma_f32_32x32x16_bf16 v[84:99], v[244:247], v[158:161], v[84:99]
	s_cbranch_vccnz .LBB0_877
	v_add_u32_e32 v2, 59, v180
	v_add_u32_e32 v164, 27, v180
	v_cmp_gt_u32_e32 vcc, s75, v2
	v_add_u32_e32 v2, 58, v180
	s_nop 5
	v_cndmask_b32_e32 v100, v226, v100, vcc
	v_cmp_gt_u32_e32 vcc, s75, v164
	v_add_u32_e32 v164, 26, v180
	s_nop 0
	v_cndmask_b32_e32 v84, v226, v84, vcc
	v_cmp_gt_u32_e32 vcc, s75, v2
	v_add_u32_e32 v2, 57, v180
	s_nop 0
	v_cndmask_b32_e32 v101, v226, v101, vcc
	v_cmp_gt_u32_e32 vcc, s75, v164
	v_add_u32_e32 v164, 25, v180
	s_nop 0
	v_cndmask_b32_e32 v85, v226, v85, vcc
	v_cmp_gt_u32_e32 vcc, s75, v2
	v_add_u32_e32 v2, 56, v180
	s_nop 0
	v_cndmask_b32_e32 v102, v226, v102, vcc
	v_cmp_gt_u32_e32 vcc, s75, v164
	v_add_u32_e32 v164, 24, v180
	s_nop 0
	v_cndmask_b32_e32 v86, v226, v86, vcc
	v_cmp_gt_u32_e32 vcc, s75, v2
	v_add_u32_e32 v2, 51, v180
	s_nop 0
	v_cndmask_b32_e32 v103, v226, v103, vcc
	v_cmp_gt_u32_e32 vcc, s75, v164
	v_add_u32_e32 v164, 19, v180
	s_nop 0
	v_cndmask_b32_e32 v87, v226, v87, vcc
	v_cmp_gt_u32_e32 vcc, s75, v2
	v_add_u32_e32 v2, 50, v180
	s_nop 0
	v_cndmask_b32_e32 v104, v226, v104, vcc
	v_cmp_gt_u32_e32 vcc, s75, v164
	v_add_u32_e32 v164, 18, v180
	s_nop 0
	v_cndmask_b32_e32 v88, v226, v88, vcc
	v_cmp_gt_u32_e32 vcc, s75, v2
	v_add_u32_e32 v2, 49, v180
	s_nop 0
	v_cndmask_b32_e32 v105, v226, v105, vcc
	v_cmp_gt_u32_e32 vcc, s75, v164
	v_add_u32_e32 v164, 17, v180
	s_nop 0
	v_cndmask_b32_e32 v89, v226, v89, vcc
	v_cmp_gt_u32_e32 vcc, s75, v2
	v_add_u32_e32 v2, 48, v180
	s_nop 0
	v_cndmask_b32_e32 v106, v226, v106, vcc
	v_cmp_gt_u32_e32 vcc, s75, v164
	v_add_u32_e32 v164, 16, v180
	s_nop 0
	v_cndmask_b32_e32 v90, v226, v90, vcc
	v_cmp_gt_u32_e32 vcc, s75, v2
	v_add_u32_e32 v2, 43, v180
	s_nop 0
	v_cndmask_b32_e32 v107, v226, v107, vcc
	v_cmp_gt_u32_e32 vcc, s75, v164
	v_add_u32_e32 v164, 11, v180
	s_nop 0
	v_cndmask_b32_e32 v91, v226, v91, vcc
	v_cmp_gt_u32_e32 vcc, s75, v2
	v_add_u32_e32 v2, 42, v180
	s_nop 0
	v_cndmask_b32_e32 v108, v226, v108, vcc
	v_cmp_gt_u32_e32 vcc, s75, v164
	v_add_u32_e32 v164, 10, v180
	s_nop 0
	v_cndmask_b32_e32 v92, v226, v92, vcc
	v_cmp_gt_u32_e32 vcc, s75, v2
	v_add_u32_e32 v2, 41, v180
	s_nop 0
	v_cndmask_b32_e32 v109, v226, v109, vcc
	v_cmp_gt_u32_e32 vcc, s75, v164
	v_add_u32_e32 v164, 9, v180
	s_nop 0
	v_cndmask_b32_e32 v93, v226, v93, vcc
	v_cmp_gt_u32_e32 vcc, s75, v2
	v_add_u32_e32 v2, 40, v180
	s_nop 0
	v_cndmask_b32_e32 v110, v226, v110, vcc
	v_cmp_gt_u32_e32 vcc, s75, v164
	v_add_u32_e32 v164, 8, v180
	s_nop 0
	v_cndmask_b32_e32 v94, v226, v94, vcc
	v_cmp_gt_u32_e32 vcc, s75, v2
	v_add_u32_e32 v2, 35, v180
	s_nop 0
	v_cndmask_b32_e32 v111, v226, v111, vcc
	v_cmp_gt_u32_e32 vcc, s75, v164
	v_add_u32_e32 v164, 3, v180
	s_nop 0
	v_cndmask_b32_e32 v95, v226, v95, vcc
	v_cmp_gt_u32_e32 vcc, s75, v2
	v_add_u32_e32 v2, 34, v180
	s_nop 0
	v_cndmask_b32_e32 v112, v226, v112, vcc
	v_cmp_gt_u32_e32 vcc, s75, v164
	v_add_u32_e32 v164, 2, v180
	s_nop 0
	v_cndmask_b32_e32 v96, v226, v96, vcc
	v_cmp_gt_u32_e32 vcc, s75, v2
	v_add_u32_e32 v2, 33, v180
	s_nop 0
	v_cndmask_b32_e32 v113, v226, v113, vcc
	v_cmp_gt_u32_e32 vcc, s75, v164
	v_add_u32_e32 v164, 1, v180
	s_nop 0
	v_cndmask_b32_e32 v97, v226, v97, vcc
	v_cmp_gt_u32_e32 vcc, s75, v2
	v_add_u32_e32 v2, 32, v180
	s_nop 0
	v_cndmask_b32_e32 v114, v226, v114, vcc
	v_cmp_gt_u32_e32 vcc, s75, v164
	s_nop 1
	v_cndmask_b32_e32 v98, v226, v98, vcc
	v_cmp_gt_u32_e32 vcc, s75, v2
	s_nop 1
	v_cndmask_b32_e32 v115, v226, v115, vcc
	v_cmp_gt_u32_e32 vcc, s75, v180
	s_nop 1
	v_cndmask_b32_e32 v99, v226, v99, vcc
